# v45 + P1 pool-mixer epilogue de-serialised: column groups 0-2 and 4-6 load together into free registers and are computed back to back with counted waits (8 exposed load latencies -> 4)
# speedup vs baseline: 1.0080x; 1.0028x over previous
.LBB0_121:
	s_min_u32 s9, s8, 3
	s_add_i32 s9, s93, s9
	s_and_b32 s9, s9, 7
	v_cndmask_b32_e64 v212, v214, 0, s[4:5]
	s_lshl_b32 s11, s9, 6
	s_waitcnt vmcnt(12) lgkmcnt(3)
	v_mfma_f32_16x16x32_bf16 v[142:145], v[66:69], v[198:201], v[142:145]
	s_waitcnt lgkmcnt(2)
	v_mfma_f32_16x16x32_bf16 v[138:141], v[66:69], v[202:205], v[138:141]
	s_waitcnt lgkmcnt(1)
	v_mfma_f32_16x16x32_bf16 v[134:137], v[66:69], v[206:209], v[134:137]
	s_waitcnt lgkmcnt(0)
	v_mfma_f32_16x16x32_bf16 v[130:133], v[66:69], v[194:197], v[130:133]
	v_sub_u32_e32 v66, s11, v212
	v_ashrrev_i32_e32 v67, 31, v66
	v_lshl_add_u64 v[66:67], v[66:67], 4, v[216:217]
	v_add_co_u32_e32 v68, vcc, s2, v66
	v_mfma_f32_16x16x32_bf16 v[158:161], v[78:81], v[198:201], v[158:161]
	s_nop 0
	v_addc_co_u32_e32 v69, vcc, 0, v67, vcc
	s_add_i32 s11, s8, s86
	v_mfma_f32_16x16x32_bf16 v[154:157], v[78:81], v[202:205], v[154:157]
	s_lshl_b32 s11, s11, 2
	s_and_b32 s11, s11, 28
	v_mfma_f32_16x16x32_bf16 v[150:153], v[78:81], v[206:209], v[150:153]
	v_mfma_f32_16x16x32_bf16 v[146:149], v[78:81], v[194:197], v[146:149]
	v_add_co_u32_e32 v78, vcc, s3, v66
	s_nop 1
	v_addc_co_u32_e32 v79, vcc, 0, v67, vcc
	v_mfma_f32_16x16x32_bf16 v[178:181], v[70:73], v[194:197], v[178:181]
	v_mfma_f32_16x16x32_bf16 v[162:165], v[74:77], v[194:197], v[162:165]
	v_add_co_u32_e32 v194, vcc, s6, v66
	v_mfma_f32_16x16x32_bf16 v[190:193], v[70:73], v[198:201], v[190:193]
	s_nop 0
	v_addc_co_u32_e32 v195, vcc, 0, v67, vcc
	v_mfma_f32_16x16x32_bf16 v[186:189], v[70:73], v[202:205], v[186:189]
	v_mfma_f32_16x16x32_bf16 v[182:185], v[70:73], v[206:209], v[182:185]
	v_mfma_f32_16x16x32_bf16 v[174:177], v[74:77], v[198:201], v[174:177]
	v_mfma_f32_16x16x32_bf16 v[170:173], v[74:77], v[202:205], v[170:173]
	v_mfma_f32_16x16x32_bf16 v[166:169], v[74:77], v[206:209], v[166:169]
	global_load_dwordx4 v[70:73], v[66:67], off
	global_load_dwordx4 v[74:77], v[68:69], off
	s_nop 0
	global_load_dwordx4 v[78:81], v[78:79], off
	s_nop 0
	global_load_dwordx4 v[66:69], v[194:195], off
	v_bitop3_b32 v194, s11, v222, v224 bitop3:0x36
	v_lshl_add_u32 v202, v194, 4, v223
	v_add_u32_e32 v203, 0x10000, v202
	v_add_u32_e32 v206, 0x18000, v202
	ds_read_b128 v[194:197], v202
	ds_read_b128 v[198:201], v202 offset:32768
	ds_read_b128 v[202:205], v203
	ds_read_b128 v[206:209], v206
	s_min_u32 s11, s8, 2
	s_add_i32 s11, s11, s88
	s_lshl_b32 s11, s11, 6
	s_and_b32 s11, s11, 0x1c0
	s_waitcnt vmcnt(15) lgkmcnt(3)
	v_mfma_f32_16x16x32_bf16 v[190:193], v[82:85], v[194:197], v[190:193]
	s_waitcnt lgkmcnt(2)
	v_mfma_f32_16x16x32_bf16 v[186:189], v[82:85], v[198:201], v[186:189]
	s_waitcnt lgkmcnt(1)
	v_mfma_f32_16x16x32_bf16 v[182:185], v[82:85], v[202:205], v[182:185]
	s_waitcnt lgkmcnt(0)
	v_mfma_f32_16x16x32_bf16 v[178:181], v[82:85], v[206:209], v[178:181]
	v_sub_u32_e32 v82, s11, v212
	v_ashrrev_i32_e32 v83, 31, v82
	v_lshl_add_u64 v[82:83], v[82:83], 4, v[216:217]
	s_waitcnt vmcnt(14)
	v_mfma_f32_16x16x32_bf16 v[174:177], v[86:89], v[194:197], v[174:177]
	s_add_i32 s11, s8, s87
	s_lshl_b32 s11, s11, 2
	s_and_b32 s11, s11, 28
	v_mfma_f32_16x16x32_bf16 v[170:173], v[86:89], v[198:201], v[170:173]
	v_mfma_f32_16x16x32_bf16 v[166:169], v[86:89], v[202:205], v[166:169]
	v_mfma_f32_16x16x32_bf16 v[162:165], v[86:89], v[206:209], v[162:165]
	v_add_co_u32_e32 v86, vcc, s2, v82
	s_nop 1
	v_addc_co_u32_e32 v87, vcc, 0, v83, vcc
	s_waitcnt vmcnt(12)
	v_mfma_f32_16x16x32_bf16 v[142:145], v[90:93], v[194:197], v[142:145]
	v_mfma_f32_16x16x32_bf16 v[138:141], v[90:93], v[198:201], v[138:141]
	v_mfma_f32_16x16x32_bf16 v[134:137], v[90:93], v[202:205], v[134:137]
	v_mfma_f32_16x16x32_bf16 v[130:133], v[90:93], v[206:209], v[130:133]
	v_add_co_u32_e32 v90, vcc, s3, v82
	s_nop 1
	v_addc_co_u32_e32 v91, vcc, 0, v83, vcc
	v_add_co_u32_e32 v92, vcc, s6, v82
	v_mfma_f32_16x16x32_bf16 v[158:161], v[94:97], v[194:197], v[158:161]
	s_nop 0
	v_addc_co_u32_e32 v93, vcc, 0, v83, vcc
	v_bitop3_b32 v194, s11, v222, v224 bitop3:0x36
	v_mfma_f32_16x16x32_bf16 v[154:157], v[94:97], v[198:201], v[154:157]
	v_mfma_f32_16x16x32_bf16 v[150:153], v[94:97], v[202:205], v[150:153]
	v_lshl_add_u32 v202, v194, 4, v223
	v_add_u32_e32 v203, 0x10000, v202
	v_mfma_f32_16x16x32_bf16 v[146:149], v[94:97], v[206:209], v[146:149]
	global_load_dwordx4 v[82:85], v[82:83], off
	s_nop 0
	global_load_dwordx4 v[86:89], v[86:87], off
	s_nop 0
	global_load_dwordx4 v[94:97], v[90:91], off
	s_nop 0
	global_load_dwordx4 v[90:93], v[92:93], off
	v_add_u32_e32 v206, 0x18000, v202
	ds_read_b128 v[194:197], v202
	ds_read_b128 v[198:201], v202 offset:32768
	ds_read_b128 v[202:205], v203
	ds_read_b128 v[206:209], v206
	s_add_i32 s8, s8, s89
	s_lshl_b32 s8, s8, 2
	s_and_b32 s8, s8, 28
	s_and_b64 vcc, s[4:5], exec
	s_cselect_b32 s4, 6, 7
	s_add_i32 s4, s4, s21
	s_lshl_b32 s4, s4, 6
	s_and_b32 s4, s4, 0x1c0
	s_waitcnt vmcnt(15) lgkmcnt(3)
	v_mfma_f32_16x16x32_bf16 v[190:193], v[98:101], v[194:197], v[190:193]
	v_bitop3_b32 v225, s8, v222, v224 bitop3:0x36
	v_lshl_add_u32 v225, v225, 4, v223
	ds_read_b128 v[226:229], v225
	ds_read_b128 v[230:233], v225 offset:32768
	s_waitcnt lgkmcnt(4)
	v_mfma_f32_16x16x32_bf16 v[186:189], v[98:101], v[198:201], v[186:189]
	v_add_u32_e32 v234, 0x10000, v225
	v_add_u32_e32 v225, 0x18000, v225
	ds_read_b128 v[234:237], v234
	ds_read_b128 v[238:241], v225
	s_waitcnt lgkmcnt(5)
	v_mfma_f32_16x16x32_bf16 v[182:185], v[98:101], v[202:205], v[182:185]
	s_waitcnt lgkmcnt(4)
	v_mfma_f32_16x16x32_bf16 v[178:181], v[98:101], v[206:209], v[178:181]
	v_sub_u32_e32 v98, s4, v212
	v_ashrrev_i32_e32 v99, 31, v98
	s_waitcnt vmcnt(12)
	v_mfma_f32_16x16x32_bf16 v[142:145], v[122:125], v[194:197], v[142:145]
	v_mfma_f32_16x16x32_bf16 v[138:141], v[122:125], v[198:201], v[138:141]
	v_mfma_f32_16x16x32_bf16 v[134:137], v[122:125], v[202:205], v[134:137]
	v_mfma_f32_16x16x32_bf16 v[130:133], v[122:125], v[206:209], v[130:133]
	v_lshl_add_u64 v[122:123], v[98:99], 4, v[216:217]
	global_load_dwordx4 v[98:101], v[122:123], off
	v_mfma_f32_16x16x32_bf16 v[174:177], v[102:105], v[194:197], v[174:177]
	v_mfma_f32_16x16x32_bf16 v[170:173], v[102:105], v[198:201], v[170:173]
	v_mfma_f32_16x16x32_bf16 v[166:169], v[102:105], v[202:205], v[166:169]
	v_mfma_f32_16x16x32_bf16 v[162:165], v[102:105], v[206:209], v[162:165]
	v_add_co_u32_e64 v102, s[4:5], s2, v122
	s_nop 1
	v_addc_co_u32_e64 v103, s[4:5], 0, v123, s[4:5]
	v_mfma_f32_16x16x32_bf16 v[158:161], v[114:117], v[194:197], v[158:161]
	global_load_dwordx4 v[102:105], v[102:103], off
	v_mfma_f32_16x16x32_bf16 v[154:157], v[114:117], v[198:201], v[154:157]
	v_mfma_f32_16x16x32_bf16 v[150:153], v[114:117], v[202:205], v[150:153]
	v_mfma_f32_16x16x32_bf16 v[146:149], v[114:117], v[206:209], v[146:149]
	v_add_co_u32_e64 v114, s[4:5], s3, v122
	s_nop 1
	v_addc_co_u32_e64 v115, s[4:5], 0, v123, s[4:5]
	v_add_co_u32_e64 v122, s[4:5], s6, v122
	global_load_dwordx4 v[114:117], v[114:115], off
	s_nop 0
	v_addc_co_u32_e64 v123, s[4:5], 0, v123, s[4:5]
	global_load_dwordx4 v[122:125], v[122:123], off
	s_waitcnt vmcnt(15) lgkmcnt(3)
	v_mfma_f32_16x16x32_bf16 v[190:193], v[106:109], v[226:229], v[190:193]
	s_lshl_b32 s4, s9, 2
	v_bitop3_b32 v194, s4, v222, v224 bitop3:0x36
	v_lshl_add_u32 v194, v194, 4, v223
	s_waitcnt lgkmcnt(2)
	v_mfma_f32_16x16x32_bf16 v[186:189], v[106:109], v[230:233], v[186:189]
	ds_read_b128 v[198:201], v194
	ds_read_b128 v[202:205], v194 offset:32768
	v_add_u32_e32 v195, 0x10000, v194
	v_add_u32_e32 v194, 0x18000, v194
	s_waitcnt lgkmcnt(3)
	v_mfma_f32_16x16x32_bf16 v[182:185], v[106:109], v[234:237], v[182:185]
	ds_read_b128 v[206:209], v195
	ds_read_b128 v[194:197], v194
	s_waitcnt lgkmcnt(4)
	v_mfma_f32_16x16x32_bf16 v[178:181], v[106:109], v[238:241], v[178:181]
	v_sub_u32_e32 v106, s90, v212
	v_ashrrev_i32_e32 v107, 31, v106
	s_waitcnt vmcnt(12)
	v_mfma_f32_16x16x32_bf16 v[142:145], v[126:129], v[226:229], v[142:145]
	v_mfma_f32_16x16x32_bf16 v[138:141], v[126:129], v[230:233], v[138:141]
	v_mfma_f32_16x16x32_bf16 v[134:137], v[126:129], v[234:237], v[134:137]
	v_mfma_f32_16x16x32_bf16 v[130:133], v[126:129], v[238:241], v[130:133]
	v_lshl_add_u64 v[126:127], v[106:107], 4, v[216:217]
	global_load_dwordx4 v[106:109], v[126:127], off
	v_mfma_f32_16x16x32_bf16 v[174:177], v[110:113], v[226:229], v[174:177]
	v_mfma_f32_16x16x32_bf16 v[170:173], v[110:113], v[230:233], v[170:173]
	v_mfma_f32_16x16x32_bf16 v[166:169], v[110:113], v[234:237], v[166:169]
	v_mfma_f32_16x16x32_bf16 v[162:165], v[110:113], v[238:241], v[162:165]
	v_add_co_u32_e64 v110, s[4:5], s2, v126
	s_nop 1
	v_addc_co_u32_e64 v111, s[4:5], 0, v127, s[4:5]
	v_mfma_f32_16x16x32_bf16 v[158:161], v[118:121], v[226:229], v[158:161]
	global_load_dwordx4 v[110:113], v[110:111], off
	v_mfma_f32_16x16x32_bf16 v[154:157], v[118:121], v[230:233], v[154:157]
	v_mfma_f32_16x16x32_bf16 v[150:153], v[118:121], v[234:237], v[150:153]
	v_mfma_f32_16x16x32_bf16 v[146:149], v[118:121], v[238:241], v[146:149]
	v_add_co_u32_e64 v118, s[4:5], s3, v126
	s_nop 1
	v_addc_co_u32_e64 v119, s[4:5], 0, v127, s[4:5]
	v_add_co_u32_e64 v126, s[4:5], s6, v126
	global_load_dwordx4 v[118:121], v[118:119], off
	s_nop 0
	v_addc_co_u32_e64 v127, s[4:5], 0, v127, s[4:5]
	global_load_dwordx4 v[126:129], v[126:127], off
	s_mov_b64 s[4:5], 0
	s_mov_b32 s8, 4
	s_cbranch_vccnz .LBB0_121
	s_lshl_b32 s4, s65, 8
	s_lshl_b32 s5, s10, 7
	s_or_b32 s29, s5, s4
	s_waitcnt vmcnt(12)
	v_lshrrev_b32_e32 v66, 2, v221
	v_and_or_b32 v66, v66, 12, s29
	v_or_b32_e32 v68, s80, v222
	v_ashrrev_i32_e32 v67, 31, v66
	s_waitcnt vmcnt(11)
	v_lshlrev_b64 v[82:83], 2, v[66:67]
	v_or_b32_e32 v66, 16, v68
	v_ashrrev_i32_e32 v67, 31, v66
	v_lshl_add_u64 v[78:79], s[70:71], 0, v[82:83]
	v_lshlrev_b64 v[66:67], 12, v[66:67]
	s_load_dwordx2 s[4:5], s[0:1], 0x10
	s_waitcnt lgkmcnt(0)
	v_lshl_add_u64 v[196:197], v[78:79], 0, v[66:67]
	v_or_b32_e32 v66, 32, v68
	v_or_b32_e32 v74, 48, v68
	v_ashrrev_i32_e32 v69, 31, v68
	v_ashrrev_i32_e32 v67, 31, v66
	v_ashrrev_i32_e32 v75, 31, v74
	v_lshlrev_b64 v[70:71], 12, v[68:69]
	v_lshlrev_b64 v[66:67], 12, v[66:67]
	v_lshlrev_b64 v[80:81], 12, v[74:75]
	v_lshl_add_u64 v[194:195], v[78:79], 0, v[70:71]
	v_lshl_add_u64 v[198:199], v[78:79], 0, v[66:67]
	v_lshl_add_u64 v[200:201], v[78:79], 0, v[80:81]
	global_load_dwordx4 v[66:69], v[194:195], off
	global_load_dwordx4 v[70:73], v[196:197], off
	global_load_dwordx4 v[74:77], v[198:199], off
	global_load_dwordx4 v[78:81], v[200:201], off
	v_lshl_add_u64 v[202:203], s[4:5], 0, v[82:83]
	global_load_dwordx4 v[82:85], v[202:203], off
	global_load_dwordx4 v[86:89], v[194:195], off offset:64
	global_load_dwordx4 v[90:93], v[196:197], off offset:64
	global_load_dwordx4 v[94:97], v[198:199], off offset:64
	global_load_dwordx4 v[98:101], v[200:201], off offset:64
	global_load_dwordx4 v[242:245], v[202:203], off offset:64
	global_load_dwordx4 v[226:229], v[194:195], off offset:128
	global_load_dwordx4 v[230:233], v[196:197], off offset:128
	global_load_dwordx4 v[234:237], v[198:199], off offset:128
	global_load_dwordx4 v[238:241], v[200:201], off offset:128
	global_load_dwordx4 v[204:207], v[202:203], off offset:128
	s_waitcnt vmcnt(14)
	v_pk_mul_f32 v[68:69], v[68:69], s[74:75] op_sel_hi:[1,0]
	v_pk_mul_f32 v[66:67], v[66:67], s[74:75] op_sel_hi:[1,0]
	s_waitcnt vmcnt(13)
	v_pk_mul_f32 v[72:73], v[72:73], s[74:75] op_sel_hi:[1,0]
	v_pk_mul_f32 v[70:71], v[70:71], s[74:75] op_sel_hi:[1,0]
	s_waitcnt vmcnt(12)
	v_pk_mul_f32 v[76:77], v[76:77], s[74:75] op_sel_hi:[1,0]
	v_pk_mul_f32 v[74:75], v[74:75], s[74:75] op_sel_hi:[1,0]
	s_waitcnt vmcnt(11)
	v_pk_mul_f32 v[80:81], v[80:81], s[74:75] op_sel_hi:[1,0]
	v_pk_mul_f32 v[78:79], v[78:79], s[74:75] op_sel_hi:[1,0]
	s_waitcnt vmcnt(10)
	v_pk_fma_f32 v[128:129], v[64:65], v[84:85], v[68:69]
	v_pk_fma_f32 v[126:127], v[62:63], v[82:83], v[66:67]
	v_pk_fma_f32 v[124:125], v[60:61], v[84:85], v[72:73]
	v_pk_fma_f32 v[122:123], v[58:59], v[82:83], v[70:71]
	v_pk_fma_f32 v[120:121], v[56:57], v[84:85], v[76:77]
	v_pk_fma_f32 v[118:119], v[54:55], v[82:83], v[74:75]
	v_pk_fma_f32 v[116:117], v[52:53], v[84:85], v[80:81]
	v_pk_fma_f32 v[114:115], v[50:51], v[82:83], v[78:79]
	s_waitcnt vmcnt(9)
	v_pk_mul_f32 v[88:89], v[88:89], s[74:75] op_sel_hi:[1,0]
	v_pk_mul_f32 v[86:87], v[86:87], s[74:75] op_sel_hi:[1,0]
	s_waitcnt vmcnt(8)
	v_pk_mul_f32 v[92:93], v[92:93], s[74:75] op_sel_hi:[1,0]
	v_pk_mul_f32 v[90:91], v[90:91], s[74:75] op_sel_hi:[1,0]
	s_waitcnt vmcnt(7)
	v_pk_mul_f32 v[96:97], v[96:97], s[74:75] op_sel_hi:[1,0]
	v_pk_mul_f32 v[94:95], v[94:95], s[74:75] op_sel_hi:[1,0]
	s_waitcnt vmcnt(6)
	v_pk_mul_f32 v[100:101], v[100:101], s[74:75] op_sel_hi:[1,0]
	v_pk_mul_f32 v[98:99], v[98:99], s[74:75] op_sel_hi:[1,0]
	s_waitcnt vmcnt(5)
	v_pk_fma_f32 v[112:113], v[48:49], v[244:245], v[88:89]
	v_pk_fma_f32 v[110:111], v[46:47], v[242:243], v[86:87]
	v_pk_fma_f32 v[108:109], v[44:45], v[244:245], v[92:93]
	v_pk_fma_f32 v[106:107], v[42:43], v[242:243], v[90:91]
	v_pk_fma_f32 v[104:105], v[40:41], v[244:245], v[96:97]
	v_pk_fma_f32 v[102:103], v[38:39], v[242:243], v[94:95]
	v_pk_fma_f32 v[100:101], v[36:37], v[244:245], v[100:101]
	v_pk_fma_f32 v[98:99], v[34:35], v[242:243], v[98:99]
	s_waitcnt vmcnt(4)
	v_pk_mul_f32 v[228:229], v[228:229], s[74:75] op_sel_hi:[1,0]
	v_pk_mul_f32 v[226:227], v[226:227], s[74:75] op_sel_hi:[1,0]
	s_waitcnt vmcnt(3)
	v_pk_mul_f32 v[232:233], v[232:233], s[74:75] op_sel_hi:[1,0]
	v_pk_mul_f32 v[230:231], v[230:231], s[74:75] op_sel_hi:[1,0]
	s_waitcnt vmcnt(2)
	v_pk_mul_f32 v[236:237], v[236:237], s[74:75] op_sel_hi:[1,0]
	v_pk_mul_f32 v[234:235], v[234:235], s[74:75] op_sel_hi:[1,0]
	s_waitcnt vmcnt(1)
	v_pk_mul_f32 v[240:241], v[240:241], s[74:75] op_sel_hi:[1,0]
	v_pk_mul_f32 v[238:239], v[238:239], s[74:75] op_sel_hi:[1,0]
	s_waitcnt vmcnt(0)
	v_pk_fma_f32 v[96:97], v[32:33], v[206:207], v[228:229]
	v_pk_fma_f32 v[94:95], v[30:31], v[204:205], v[226:227]
	v_pk_fma_f32 v[92:93], v[28:29], v[206:207], v[232:233]
	v_pk_fma_f32 v[90:91], v[26:27], v[204:205], v[230:231]
	v_pk_fma_f32 v[88:89], v[24:25], v[206:207], v[236:237]
	v_pk_fma_f32 v[86:87], v[22:23], v[204:205], v[234:235]
	v_pk_fma_f32 v[84:85], v[20:21], v[206:207], v[240:241]
	v_pk_fma_f32 v[82:83], v[18:19], v[204:205], v[238:239]
	s_nop 0
	global_load_dwordx4 v[18:21], v[194:195], off offset:192
	global_load_dwordx4 v[22:25], v[196:197], off offset:192
	global_load_dwordx4 v[26:29], v[198:199], off offset:192
	global_load_dwordx4 v[30:33], v[200:201], off offset:192
	global_load_dwordx4 v[34:37], v[202:203], off offset:192
	s_waitcnt vmcnt(4)
	v_pk_mul_f32 v[20:21], v[20:21], s[74:75] op_sel_hi:[1,0]
	v_pk_mul_f32 v[18:19], v[18:19], s[74:75] op_sel_hi:[1,0]
	s_waitcnt vmcnt(3)
	v_pk_mul_f32 v[24:25], v[24:25], s[74:75] op_sel_hi:[1,0]
	v_pk_mul_f32 v[22:23], v[22:23], s[74:75] op_sel_hi:[1,0]
	s_waitcnt vmcnt(2)
	v_pk_mul_f32 v[28:29], v[28:29], s[74:75] op_sel_hi:[1,0]
	v_pk_mul_f32 v[26:27], v[26:27], s[74:75] op_sel_hi:[1,0]
	s_waitcnt vmcnt(1)
	v_pk_mul_f32 v[32:33], v[32:33], s[74:75] op_sel_hi:[1,0]
	v_pk_mul_f32 v[30:31], v[30:31], s[74:75] op_sel_hi:[1,0]
	s_waitcnt vmcnt(0)
	v_pk_fma_f32 v[80:81], v[16:17], v[36:37], v[20:21]
	v_pk_fma_f32 v[78:79], v[14:15], v[34:35], v[18:19]
	v_pk_fma_f32 v[76:77], v[12:13], v[36:37], v[24:25]
	v_pk_fma_f32 v[74:75], v[10:11], v[34:35], v[22:23]
	v_pk_fma_f32 v[72:73], v[8:9], v[36:37], v[28:29]
	v_pk_fma_f32 v[70:71], v[6:7], v[34:35], v[26:27]
	v_pk_fma_f32 v[68:69], v[4:5], v[36:37], v[32:33]
	v_pk_fma_f32 v[66:67], v[2:3], v[34:35], v[30:31]
	s_nop 0
	global_load_dwordx4 v[2:5], v[194:195], off offset:256
	global_load_dwordx4 v[6:9], v[196:197], off offset:256
	global_load_dwordx4 v[10:13], v[198:199], off offset:256
	global_load_dwordx4 v[14:17], v[200:201], off offset:256
	global_load_dwordx4 v[18:21], v[202:203], off offset:256
	global_load_dwordx4 v[22:25], v[194:195], off offset:320
	global_load_dwordx4 v[26:29], v[196:197], off offset:320
	global_load_dwordx4 v[30:33], v[198:199], off offset:320
	global_load_dwordx4 v[34:37], v[200:201], off offset:320
	global_load_dwordx4 v[242:245], v[202:203], off offset:320
	global_load_dwordx4 v[226:229], v[194:195], off offset:384
	global_load_dwordx4 v[230:233], v[196:197], off offset:384
	global_load_dwordx4 v[234:237], v[198:199], off offset:384
	global_load_dwordx4 v[238:241], v[200:201], off offset:384
	global_load_dwordx4 v[204:207], v[202:203], off offset:384
	s_waitcnt vmcnt(14)
	v_pk_mul_f32 v[4:5], v[4:5], s[74:75] op_sel_hi:[1,0]
	v_pk_mul_f32 v[2:3], v[2:3], s[74:75] op_sel_hi:[1,0]
	s_waitcnt vmcnt(13)
	v_pk_mul_f32 v[8:9], v[8:9], s[74:75] op_sel_hi:[1,0]
	v_pk_mul_f32 v[6:7], v[6:7], s[74:75] op_sel_hi:[1,0]
	s_waitcnt vmcnt(12)
	v_pk_mul_f32 v[12:13], v[12:13], s[74:75] op_sel_hi:[1,0]
	v_pk_mul_f32 v[10:11], v[10:11], s[74:75] op_sel_hi:[1,0]
	s_waitcnt vmcnt(11)
	v_pk_mul_f32 v[16:17], v[16:17], s[74:75] op_sel_hi:[1,0]
	v_pk_mul_f32 v[14:15], v[14:15], s[74:75] op_sel_hi:[1,0]
	s_waitcnt vmcnt(10)
	v_pk_fma_f32 v[64:65], v[192:193], v[20:21], v[4:5]
	v_pk_fma_f32 v[62:63], v[190:191], v[18:19], v[2:3]
	v_pk_fma_f32 v[56:57], v[188:189], v[20:21], v[8:9]
	v_pk_fma_f32 v[54:55], v[186:187], v[18:19], v[6:7]
	v_pk_fma_f32 v[48:49], v[184:185], v[20:21], v[12:13]
	v_pk_fma_f32 v[46:47], v[182:183], v[18:19], v[10:11]
	v_pk_fma_f32 v[40:41], v[180:181], v[20:21], v[16:17]
	v_pk_fma_f32 v[38:39], v[178:179], v[18:19], v[14:15]
	s_waitcnt vmcnt(9)
	v_pk_mul_f32 v[24:25], v[24:25], s[74:75] op_sel_hi:[1,0]
	v_pk_mul_f32 v[22:23], v[22:23], s[74:75] op_sel_hi:[1,0]
	s_waitcnt vmcnt(8)
	v_pk_mul_f32 v[28:29], v[28:29], s[74:75] op_sel_hi:[1,0]
	v_pk_mul_f32 v[26:27], v[26:27], s[74:75] op_sel_hi:[1,0]
	s_waitcnt vmcnt(7)
	v_pk_mul_f32 v[32:33], v[32:33], s[74:75] op_sel_hi:[1,0]
	v_pk_mul_f32 v[30:31], v[30:31], s[74:75] op_sel_hi:[1,0]
	s_waitcnt vmcnt(6)
	v_pk_mul_f32 v[36:37], v[36:37], s[74:75] op_sel_hi:[1,0]
	v_pk_mul_f32 v[34:35], v[34:35], s[74:75] op_sel_hi:[1,0]
	s_waitcnt vmcnt(5)
	v_pk_fma_f32 v[60:61], v[176:177], v[244:245], v[24:25]
	v_pk_fma_f32 v[58:59], v[174:175], v[242:243], v[22:23]
	v_pk_fma_f32 v[52:53], v[172:173], v[244:245], v[28:29]
	v_pk_fma_f32 v[50:51], v[170:171], v[242:243], v[26:27]
	v_pk_fma_f32 v[44:45], v[168:169], v[244:245], v[32:33]
	v_pk_fma_f32 v[42:43], v[166:167], v[242:243], v[30:31]
	v_pk_fma_f32 v[24:25], v[164:165], v[244:245], v[36:37]
	v_pk_fma_f32 v[22:23], v[162:163], v[242:243], v[34:35]
	s_waitcnt vmcnt(4)
	v_pk_mul_f32 v[228:229], v[228:229], s[74:75] op_sel_hi:[1,0]
	v_pk_mul_f32 v[226:227], v[226:227], s[74:75] op_sel_hi:[1,0]
	s_waitcnt vmcnt(3)
	v_pk_mul_f32 v[232:233], v[232:233], s[74:75] op_sel_hi:[1,0]
	v_pk_mul_f32 v[230:231], v[230:231], s[74:75] op_sel_hi:[1,0]
	s_waitcnt vmcnt(2)
	v_pk_mul_f32 v[236:237], v[236:237], s[74:75] op_sel_hi:[1,0]
	v_pk_mul_f32 v[234:235], v[234:235], s[74:75] op_sel_hi:[1,0]
	s_waitcnt vmcnt(1)
	v_pk_mul_f32 v[240:241], v[240:241], s[74:75] op_sel_hi:[1,0]
	v_pk_mul_f32 v[238:239], v[238:239], s[74:75] op_sel_hi:[1,0]
	s_waitcnt vmcnt(0)
	v_pk_fma_f32 v[36:37], v[160:161], v[206:207], v[228:229]
	v_pk_fma_f32 v[34:35], v[158:159], v[204:205], v[226:227]
	v_pk_fma_f32 v[32:33], v[156:157], v[206:207], v[232:233]
	v_pk_fma_f32 v[30:31], v[154:155], v[204:205], v[230:231]
	v_pk_fma_f32 v[28:29], v[152:153], v[206:207], v[236:237]
	v_pk_fma_f32 v[26:27], v[150:151], v[204:205], v[234:235]
	v_pk_fma_f32 v[20:21], v[148:149], v[206:207], v[240:241]
	v_pk_fma_f32 v[18:19], v[146:147], v[204:205], v[238:239]
	v_and_b32_e32 v153, 64, v215
	global_load_dwordx4 v[2:5], v[194:195], off offset:448
	global_load_dwordx4 v[6:9], v[196:197], off offset:448
	global_load_dwordx4 v[10:13], v[198:199], off offset:448
	global_load_dwordx4 v[14:17], v[200:201], off offset:448
	global_load_dwordx4 v[154:157], v[202:203], off offset:448
	v_xor_b32_e32 v146, 16, v215
	v_add_u32_e32 v149, 64, v153
	v_xor_b32_e32 v147, 32, v215
	v_cmp_lt_i32_e32 vcc, v146, v149
	v_fma_f32 v151, v126, v126, 0
	v_fmac_f32_e32 v151, v127, v127
	v_cndmask_b32_e32 v146, v215, v146, vcc
	v_cmp_lt_i32_e32 vcc, v147, v149
	v_fmac_f32_e32 v151, v128, v128
	v_fmac_f32_e32 v151, v129, v129
	v_cndmask_b32_e32 v148, v215, v147, vcc
	v_lshlrev_b32_e32 v147, 2, v146
	v_lshlrev_b32_e32 v146, 2, v148
	v_add_f32_e32 v148, 0, v126
	v_add_f32_e32 v148, v127, v148
	v_add_f32_e32 v148, v128, v148
	v_add_f32_e32 v148, v129, v148
	v_add_f32_e32 v148, v148, v110
	v_fmac_f32_e32 v151, v110, v110
	v_add_f32_e32 v148, v111, v148
	v_fmac_f32_e32 v151, v111, v111
	v_add_f32_e32 v148, v112, v148
	v_fmac_f32_e32 v151, v112, v112
	v_add_f32_e32 v148, v113, v148
	v_fmac_f32_e32 v151, v113, v113
	v_add_f32_e32 v148, v148, v94
	v_fmac_f32_e32 v151, v94, v94
	v_add_f32_e32 v148, v95, v148
	v_fmac_f32_e32 v151, v95, v95
	v_add_f32_e32 v148, v96, v148
	v_fmac_f32_e32 v151, v96, v96
	v_add_f32_e32 v148, v97, v148
	v_fmac_f32_e32 v151, v97, v97
	v_add_f32_e32 v148, v148, v78
	v_fmac_f32_e32 v151, v78, v78
	v_add_f32_e32 v148, v79, v148
	v_fmac_f32_e32 v151, v79, v79
	v_add_f32_e32 v148, v80, v148
	v_fmac_f32_e32 v151, v80, v80
	v_add_f32_e32 v148, v81, v148
	v_fmac_f32_e32 v151, v81, v81
	v_add_f32_e32 v148, v148, v62
	v_fmac_f32_e32 v151, v62, v62
	v_add_f32_e32 v148, v63, v148
	v_fmac_f32_e32 v151, v63, v63
	v_add_f32_e32 v148, v64, v148
	v_fmac_f32_e32 v151, v64, v64
	v_add_f32_e32 v148, v65, v148
	v_fmac_f32_e32 v151, v65, v65
	v_add_f32_e32 v148, v148, v58
	v_fmac_f32_e32 v151, v58, v58
	v_add_f32_e32 v148, v59, v148
	v_fmac_f32_e32 v151, v59, v59
	v_add_f32_e32 v148, v60, v148
	v_fmac_f32_e32 v151, v60, v60
	v_add_f32_e32 v148, v61, v148
	v_fmac_f32_e32 v151, v61, v61
	v_add_f32_e32 v148, v148, v34
	v_fmac_f32_e32 v151, v34, v34
	v_add_f32_e32 v148, v35, v148
	v_fmac_f32_e32 v151, v35, v35
	v_add_f32_e32 v148, v36, v148
	v_fmac_f32_e32 v151, v36, v36
	v_add_f32_e32 v148, v37, v148
	v_fmac_f32_e32 v151, v37, v37
	s_waitcnt vmcnt(4)
	v_pk_mul_f32 v[4:5], v[4:5], s[74:75] op_sel_hi:[1,0]
	v_pk_mul_f32 v[2:3], v[2:3], s[74:75] op_sel_hi:[1,0]
	s_waitcnt vmcnt(3)
	v_pk_mul_f32 v[8:9], v[8:9], s[74:75] op_sel_hi:[1,0]
	s_waitcnt vmcnt(1)
	v_pk_mul_f32 v[162:163], v[16:17], s[74:75] op_sel_hi:[1,0]
	v_pk_mul_f32 v[164:165], v[14:15], s[74:75] op_sel_hi:[1,0]
	s_waitcnt vmcnt(0)
	v_pk_fma_f32 v[16:17], v[144:145], v[156:157], v[4:5]
	v_pk_fma_f32 v[14:15], v[142:143], v[154:155], v[2:3]
	v_pk_fma_f32 v[2:3], v[130:131], v[154:155], v[164:165]
	v_pk_mul_f32 v[6:7], v[6:7], s[74:75] op_sel_hi:[1,0]
	v_add_f32_e32 v130, v148, v14
	v_fmac_f32_e32 v151, v14, v14
	v_add_f32_e32 v130, v15, v130
	v_fmac_f32_e32 v151, v15, v15
	v_add_f32_e32 v130, v16, v130
	v_fmac_f32_e32 v151, v16, v16
	v_add_f32_e32 v150, v17, v130
	v_fmac_f32_e32 v151, v17, v17
	ds_bpermute_b32 v130, v147, v150
	ds_bpermute_b32 v131, v147, v151
	v_pk_mul_f32 v[158:159], v[12:13], s[74:75] op_sel_hi:[1,0]
	v_pk_mul_f32 v[160:161], v[10:11], s[74:75] op_sel_hi:[1,0]
	v_pk_fma_f32 v[4:5], v[132:133], v[156:157], v[162:163]
	v_pk_fma_f32 v[12:13], v[140:141], v[156:157], v[8:9]
	s_waitcnt lgkmcnt(0)
	v_pk_add_f32 v[130:131], v[150:151], v[130:131]
	ds_bpermute_b32 v132, v146, v130
	ds_bpermute_b32 v133, v146, v131
	v_pk_fma_f32 v[10:11], v[138:139], v[154:155], v[6:7]
	v_pk_fma_f32 v[8:9], v[136:137], v[156:157], v[158:159]
	v_pk_fma_f32 v[6:7], v[134:135], v[154:155], v[160:161]
	s_nop 0
	s_nop 0
	v_readfirstlane_b32 s11, v221
	v_and_b32_e32 v141, 63, v221
	s_ashr_i32 s10, s11, 6
	v_cmp_lt_u32_e32 vcc, 15, v141
	v_cmp_gt_u32_e64 s[4:5], 16, v141
	s_and_saveexec_b64 s[8:9], s[4:5]
	s_cbranch_execz .LBB0_124
	s_lshl_b32 s31, s10, 9
	s_add_i32 s31, s31, 0
	v_lshl_add_u32 v134, v141, 3, s31
	v_add_u32_e32 v134, 0x20000, v134
	s_waitcnt lgkmcnt(0)
	v_pk_add_f32 v[130:131], v[130:131], v[132:133]
	ds_write_b64 v134, v[130:131]
